# speedup vs baseline: 1.0449x; 1.0013x over previous
.Lk_144:
	v_or_b32_e32 v46, 0x400, v54
	buffer_load_dwordx4 v[46:49], v46, s[4:7], 0 offen sc1
	ds_read_b128 v[50:53], v1
	v_mov_b32_e32 v66, 0
	v_add_u32_e32 v63, 0x800, v54
	s_mov_b32 s9, 0
	v_mov_b32_e32 v67, 0
	v_mov_b32_e32 v68, 0
	v_mov_b32_e32 v62, 0xc038aa3b
	s_mov_b32 s8, 0x4038aa3b
	v_mov_b32_e32 v65, 0
	v_mov_b32_e32 v64, v66
	s_setprio 2
	v_mov_b32_e32 v92, 0xc038aa3b
	v_mov_b32_e32 v93, 0xc038aa3b
	s_mov_b32 s8, 0x4038aa3b
	s_mov_b32 s9, 0
	v_mov_b32_e32 v64, 0
	v_mov_b32_e32 v65, 0
	v_mov_b32_e32 v66, 0
	v_mov_b32_e32 v67, 0
	v_mov_b32_e32 v68, 0
	v_mov_b32_e32 v116, v1
	v_mov_b32_e32 v117, v63
	s_mov_b32 s12, 0
	s_waitcnt lgkmcnt(0)
	s_setprio 2
	v_mfma_f32_16x16x32_f16 v[84:87], v[6:9], v[50:53], v[18:21]
	v_mfma_f32_16x16x32_f16 v[88:91], v[10:13], v[50:53], v[38:41]
	ds_read_b128 v[56:59], v75 offset:2048
	ds_read_b128 v[60:63], v75 offset:3072
	s_waitcnt vmcnt(1)
	v_mfma_f32_16x16x32_f16 v[84:87], v[2:5], v[42:45], v[84:87]
	v_mfma_f32_16x16x32_f16 v[88:91], v[14:17], v[42:45], v[88:91]
	v_readfirstlane_b32 s10, v67
	v_readfirstlane_b32 s11, v68
	global_load_dword v67, v66, s[0:1] sc1
	global_load_dword v68, v66, s[0:1] offset:4 sc1
	s_min_u32 s10, s10, s11
	s_max_u32 s14, s14, s10
	s_waitcnt lgkmcnt(1)
	v_mfma_f32_16x16x32_f16 v[84:87], v[30:33], v[56:59], v[84:87]
	v_mfma_f32_16x16x32_f16 v[88:91], v[22:25], v[56:59], v[88:91]
	s_waitcnt lgkmcnt(0)
	v_mfma_f32_16x16x32_f16 v[84:87], v[34:37], v[60:63], v[84:87]
	v_mfma_f32_16x16x32_f16 v[88:91], v[26:29], v[60:63], v[88:91]
	s_add_u32 s13, s12, 3
	s_min_u32 s13, s13, 450
	s_cmp_ge_u32 s14, s13
	s_cbranch_scc0 .Lca_slow_3
.Lca_ok_1:
	buffer_load_dwordx4 v[42:45], v117, s[4:7], 0 offen offset:0 sc1
	ds_read_b128 v[50:53], v116 offset:256
	s_setprio 0
	v_exp_f32_e32 v94, v86
	v_exp_f32_e32 v95, v90
	v_exp_f32_e32 v96, v84
	v_exp_f32_e32 v97, v88
	v_exp_f32_e32 v98, v85
	v_exp_f32_e32 v99, v89
	v_pk_add_f32 v[100:101], v[94:95], 1.0 op_sel_hi:[1,0]
	v_pk_fma_f32 v[102:103], v[94:95], s[8:9], v[92:93] op_sel_hi:[1,0,0]
	v_pk_fma_f32 v[100:101], v[96:97], v[100:101], v[100:101]
	v_pk_fma_f32 v[104:105], v[100:101], v[98:99], v[100:101]
	v_rcp_f32_e32 v104, v104
	v_rcp_f32_e32 v105, v105
	v_pk_fma_f32 v[102:103], v[102:103], v[98:99], v[102:103]
	v_pk_fma_f32 v[102:103], v[64:65], v[100:101], v[102:103]
	v_exp_f32_e32 v106, v87
	v_pk_mul_f32 v[64:65], v[102:103], v[104:105]
	v_exp_f32_e32 v108, v64
	v_exp_f32_e32 v109, v65
	v_exp_f32_e32 v107, v91
	v_pk_add_f32 v[110:111], v[108:109], 1.0 op_sel_hi:[1,0]
	v_pk_fma_f32 v[110:111], v[110:111], v[106:107], v[110:111]
	v_rcp_f32_e32 v110, v110
	v_rcp_f32_e32 v111, v111
	v_pk_add_f32 v[112:113], v[108:109], -1.0 op_sel_hi:[1,0]
	v_pk_mul_f32 v[112:113], v[112:113], v[110:111]
	v_cvt_pk_f16_f32 v114, v112, v113
	ds_write_b32 v81, v114 offset:0
	s_waitcnt lgkmcnt(0)
	s_barrier
	s_setprio 2
	v_mfma_f32_16x16x32_f16 v[84:87], v[6:9], v[50:53], v[18:21]
	v_mfma_f32_16x16x32_f16 v[88:91], v[10:13], v[50:53], v[38:41]
	ds_read_b128 v[56:59], v75 offset:0
	ds_read_b128 v[60:63], v75 offset:1024
	s_waitcnt vmcnt(3)
	v_mfma_f32_16x16x32_f16 v[84:87], v[2:5], v[46:49], v[84:87]
	v_mfma_f32_16x16x32_f16 v[88:91], v[14:17], v[46:49], v[88:91]
	s_waitcnt lgkmcnt(1)
	v_mfma_f32_16x16x32_f16 v[84:87], v[30:33], v[56:59], v[84:87]
	v_mfma_f32_16x16x32_f16 v[88:91], v[22:25], v[56:59], v[88:91]
	s_waitcnt lgkmcnt(0)
	v_mfma_f32_16x16x32_f16 v[84:87], v[34:37], v[60:63], v[84:87]
	v_mfma_f32_16x16x32_f16 v[88:91], v[26:29], v[60:63], v[88:91]
	s_add_u32 s13, s12, 4
	s_min_u32 s13, s13, 450
	s_cmp_ge_u32 s14, s13
	s_cbranch_scc0 .Lca_slow_6
.Lca_ok_4:
	buffer_load_dwordx4 v[46:49], v117, s[4:7], 0 offen offset:1024 sc1
	ds_read_b128 v[50:53], v116 offset:512
	s_setprio 0
	v_exp_f32_e32 v94, v86
	v_exp_f32_e32 v95, v90
	v_exp_f32_e32 v96, v84
	v_exp_f32_e32 v97, v88
	v_exp_f32_e32 v98, v85
	v_exp_f32_e32 v99, v89
	v_pk_add_f32 v[100:101], v[94:95], 1.0 op_sel_hi:[1,0]
	v_pk_fma_f32 v[102:103], v[94:95], s[8:9], v[92:93] op_sel_hi:[1,0,0]
	v_pk_fma_f32 v[100:101], v[96:97], v[100:101], v[100:101]
	v_pk_fma_f32 v[104:105], v[100:101], v[98:99], v[100:101]
	v_rcp_f32_e32 v104, v104
	v_rcp_f32_e32 v105, v105
	v_pk_fma_f32 v[102:103], v[102:103], v[98:99], v[102:103]
	v_pk_fma_f32 v[102:103], v[64:65], v[100:101], v[102:103]
	v_exp_f32_e32 v106, v87
	v_pk_mul_f32 v[64:65], v[102:103], v[104:105]
	v_exp_f32_e32 v108, v64
	v_exp_f32_e32 v109, v65
	v_exp_f32_e32 v107, v91
	v_pk_add_f32 v[110:111], v[108:109], 1.0 op_sel_hi:[1,0]
	v_pk_fma_f32 v[110:111], v[110:111], v[106:107], v[110:111]
	v_rcp_f32_e32 v110, v110
	v_rcp_f32_e32 v111, v111
	v_pk_add_f32 v[112:113], v[108:109], -1.0 op_sel_hi:[1,0]
	v_pk_mul_f32 v[112:113], v[112:113], v[110:111]
	v_cvt_pk_f16_f32 v114, v112, v113
	ds_write_b32 v81, v114 offset:2048
	s_waitcnt lgkmcnt(0)
	v_add_u32_e32 v116, 0x200, v116
	v_add_u32_e32 v117, 0x800, v117
	s_mov_b32 s12, 2
	.p2align	6
.Lca_loop:
	s_barrier
	s_setprio 2
	v_mfma_f32_16x16x32_f16 v[84:87], v[6:9], v[50:53], v[18:21]
	v_mfma_f32_16x16x32_f16 v[88:91], v[10:13], v[50:53], v[38:41]
	ds_read_b128 v[56:59], v75 offset:2048
	ds_read_b128 v[60:63], v75 offset:3072
	s_waitcnt vmcnt(1)
	v_mfma_f32_16x16x32_f16 v[84:87], v[2:5], v[42:45], v[84:87]
	v_mfma_f32_16x16x32_f16 v[88:91], v[14:17], v[42:45], v[88:91]
	v_readfirstlane_b32 s10, v67
	v_readfirstlane_b32 s11, v68
	global_load_dword v67, v66, s[0:1] sc1
	global_load_dword v68, v66, s[0:1] offset:4 sc1
	s_min_u32 s10, s10, s11
	s_max_u32 s14, s14, s10
	s_waitcnt lgkmcnt(1)
	v_mfma_f32_16x16x32_f16 v[84:87], v[30:33], v[56:59], v[84:87]
	v_mfma_f32_16x16x32_f16 v[88:91], v[22:25], v[56:59], v[88:91]
	s_waitcnt lgkmcnt(0)
	v_mfma_f32_16x16x32_f16 v[84:87], v[34:37], v[60:63], v[84:87]
	v_mfma_f32_16x16x32_f16 v[88:91], v[26:29], v[60:63], v[88:91]
	s_add_u32 s13, s12, 3
	s_min_u32 s13, s13, 450
	s_cmp_ge_u32 s14, s13
	s_cbranch_scc0 .Lca_slow_9
.Lca_ok_7:
	buffer_load_dwordx4 v[42:45], v117, s[4:7], 0 offen offset:0 sc1
	ds_read_b128 v[50:53], v116 offset:256
	s_setprio 0
	v_min_f32_e32 v64, 0x42700000, v64
	v_min_f32_e32 v65, 0x42700000, v65
	v_exp_f32_e32 v94, v86
	v_exp_f32_e32 v95, v90
	v_exp_f32_e32 v96, v84
	v_exp_f32_e32 v97, v88
	v_exp_f32_e32 v98, v85
	v_exp_f32_e32 v99, v89
	v_pk_add_f32 v[100:101], v[94:95], 1.0 op_sel_hi:[1,0]
	v_pk_fma_f32 v[102:103], v[94:95], s[8:9], v[92:93] op_sel_hi:[1,0,0]
	v_pk_fma_f32 v[100:101], v[96:97], v[100:101], v[100:101]
	v_pk_fma_f32 v[104:105], v[100:101], v[98:99], v[100:101]
	v_rcp_f32_e32 v104, v104
	v_rcp_f32_e32 v105, v105
	v_pk_fma_f32 v[102:103], v[102:103], v[98:99], v[102:103]
	v_pk_fma_f32 v[102:103], v[64:65], v[100:101], v[102:103]
	v_exp_f32_e32 v106, v87
	v_pk_mul_f32 v[64:65], v[102:103], v[104:105]
	v_exp_f32_e32 v108, v64
	v_exp_f32_e32 v109, v65
	v_exp_f32_e32 v107, v91
	v_pk_add_f32 v[110:111], v[108:109], 1.0 op_sel_hi:[1,0]
	v_pk_fma_f32 v[110:111], v[110:111], v[106:107], v[110:111]
	v_rcp_f32_e32 v110, v110
	v_rcp_f32_e32 v111, v111
	v_pk_add_f32 v[112:113], v[108:109], -1.0 op_sel_hi:[1,0]
	v_pk_mul_f32 v[112:113], v[112:113], v[110:111]
	v_cvt_pk_f16_f32 v114, v112, v113
	ds_write_b32 v81, v114 offset:0
	s_waitcnt lgkmcnt(0)
	s_barrier
	s_setprio 2
	v_mfma_f32_16x16x32_f16 v[84:87], v[6:9], v[50:53], v[18:21]
	v_mfma_f32_16x16x32_f16 v[88:91], v[10:13], v[50:53], v[38:41]
	ds_read_b128 v[56:59], v75 offset:0
	ds_read_b128 v[60:63], v75 offset:1024
	s_waitcnt vmcnt(3)
	v_mfma_f32_16x16x32_f16 v[84:87], v[2:5], v[46:49], v[84:87]
	v_mfma_f32_16x16x32_f16 v[88:91], v[14:17], v[46:49], v[88:91]
	s_waitcnt lgkmcnt(1)
	v_mfma_f32_16x16x32_f16 v[84:87], v[30:33], v[56:59], v[84:87]
	v_mfma_f32_16x16x32_f16 v[88:91], v[22:25], v[56:59], v[88:91]
	s_waitcnt lgkmcnt(0)
	v_mfma_f32_16x16x32_f16 v[84:87], v[34:37], v[60:63], v[84:87]
	v_mfma_f32_16x16x32_f16 v[88:91], v[26:29], v[60:63], v[88:91]
	s_add_u32 s13, s12, 4
	s_min_u32 s13, s13, 450
	s_cmp_ge_u32 s14, s13
	s_cbranch_scc0 .Lca_slow_12
.Lca_ok_10:
	buffer_load_dwordx4 v[46:49], v117, s[4:7], 0 offen offset:1024 sc1
	ds_read_b128 v[50:53], v116 offset:512
	s_setprio 0
	v_exp_f32_e32 v94, v86
	v_exp_f32_e32 v95, v90
	v_exp_f32_e32 v96, v84
	v_exp_f32_e32 v97, v88
	v_exp_f32_e32 v98, v85
	v_exp_f32_e32 v99, v89
	v_pk_add_f32 v[100:101], v[94:95], 1.0 op_sel_hi:[1,0]
	v_pk_fma_f32 v[102:103], v[94:95], s[8:9], v[92:93] op_sel_hi:[1,0,0]
	v_pk_fma_f32 v[100:101], v[96:97], v[100:101], v[100:101]
	v_pk_fma_f32 v[104:105], v[100:101], v[98:99], v[100:101]
	v_rcp_f32_e32 v104, v104
	v_rcp_f32_e32 v105, v105
	v_pk_fma_f32 v[102:103], v[102:103], v[98:99], v[102:103]
	v_pk_fma_f32 v[102:103], v[64:65], v[100:101], v[102:103]
	v_exp_f32_e32 v106, v87
	v_pk_mul_f32 v[64:65], v[102:103], v[104:105]
	v_exp_f32_e32 v108, v64
	v_exp_f32_e32 v109, v65
	v_exp_f32_e32 v107, v91
	v_pk_add_f32 v[110:111], v[108:109], 1.0 op_sel_hi:[1,0]
	v_pk_fma_f32 v[110:111], v[110:111], v[106:107], v[110:111]
	v_rcp_f32_e32 v110, v110
	v_rcp_f32_e32 v111, v111
	v_pk_add_f32 v[112:113], v[108:109], -1.0 op_sel_hi:[1,0]
	v_pk_mul_f32 v[112:113], v[112:113], v[110:111]
	v_cvt_pk_f16_f32 v114, v112, v113
	ds_write_b32 v81, v114 offset:2048
	s_waitcnt lgkmcnt(0)
	s_barrier
	s_setprio 2
	v_mfma_f32_16x16x32_f16 v[84:87], v[6:9], v[50:53], v[18:21]
	v_mfma_f32_16x16x32_f16 v[88:91], v[10:13], v[50:53], v[38:41]
	ds_read_b128 v[56:59], v75 offset:2048
	ds_read_b128 v[60:63], v75 offset:3072
	s_waitcnt vmcnt(1)
	v_mfma_f32_16x16x32_f16 v[84:87], v[2:5], v[42:45], v[84:87]
	v_mfma_f32_16x16x32_f16 v[88:91], v[14:17], v[42:45], v[88:91]
	v_readfirstlane_b32 s10, v67
	v_readfirstlane_b32 s11, v68
	global_load_dword v67, v66, s[0:1] sc1
	global_load_dword v68, v66, s[0:1] offset:4 sc1
	s_min_u32 s10, s10, s11
	s_max_u32 s14, s14, s10
	s_waitcnt lgkmcnt(1)
	v_mfma_f32_16x16x32_f16 v[84:87], v[30:33], v[56:59], v[84:87]
	v_mfma_f32_16x16x32_f16 v[88:91], v[22:25], v[56:59], v[88:91]
	s_waitcnt lgkmcnt(0)
	v_mfma_f32_16x16x32_f16 v[84:87], v[34:37], v[60:63], v[84:87]
	v_mfma_f32_16x16x32_f16 v[88:91], v[26:29], v[60:63], v[88:91]
	s_add_u32 s13, s12, 5
	s_min_u32 s13, s13, 450
	s_cmp_ge_u32 s14, s13
	s_cbranch_scc0 .Lca_slow_15
.Lca_ok_13:
	buffer_load_dwordx4 v[42:45], v117, s[4:7], 0 offen offset:2048 sc1
	ds_read_b128 v[50:53], v116 offset:768
	s_setprio 0
	v_exp_f32_e32 v94, v86
	v_exp_f32_e32 v95, v90
	v_exp_f32_e32 v96, v84
	v_exp_f32_e32 v97, v88
	v_exp_f32_e32 v98, v85
	v_exp_f32_e32 v99, v89
	v_pk_add_f32 v[100:101], v[94:95], 1.0 op_sel_hi:[1,0]
	v_pk_fma_f32 v[102:103], v[94:95], s[8:9], v[92:93] op_sel_hi:[1,0,0]
	v_pk_fma_f32 v[100:101], v[96:97], v[100:101], v[100:101]
	v_pk_fma_f32 v[104:105], v[100:101], v[98:99], v[100:101]
	v_rcp_f32_e32 v104, v104
	v_rcp_f32_e32 v105, v105
	v_pk_fma_f32 v[102:103], v[102:103], v[98:99], v[102:103]
	v_pk_fma_f32 v[102:103], v[64:65], v[100:101], v[102:103]
	v_exp_f32_e32 v106, v87
	v_pk_mul_f32 v[64:65], v[102:103], v[104:105]
	v_exp_f32_e32 v108, v64
	v_exp_f32_e32 v109, v65
	v_exp_f32_e32 v107, v91
	v_pk_add_f32 v[110:111], v[108:109], 1.0 op_sel_hi:[1,0]
	v_pk_fma_f32 v[110:111], v[110:111], v[106:107], v[110:111]
	v_rcp_f32_e32 v110, v110
	v_rcp_f32_e32 v111, v111
	v_pk_add_f32 v[112:113], v[108:109], -1.0 op_sel_hi:[1,0]
	v_pk_mul_f32 v[112:113], v[112:113], v[110:111]
	v_cvt_pk_f16_f32 v114, v112, v113
	ds_write_b32 v81, v114 offset:0
	s_waitcnt lgkmcnt(0)
	s_barrier
	s_setprio 2
	v_mfma_f32_16x16x32_f16 v[84:87], v[6:9], v[50:53], v[18:21]
	v_mfma_f32_16x16x32_f16 v[88:91], v[10:13], v[50:53], v[38:41]
	ds_read_b128 v[56:59], v75 offset:0
	ds_read_b128 v[60:63], v75 offset:1024
	s_waitcnt vmcnt(3)
	v_mfma_f32_16x16x32_f16 v[84:87], v[2:5], v[46:49], v[84:87]
	v_mfma_f32_16x16x32_f16 v[88:91], v[14:17], v[46:49], v[88:91]
	s_waitcnt lgkmcnt(1)
	v_mfma_f32_16x16x32_f16 v[84:87], v[30:33], v[56:59], v[84:87]
	v_mfma_f32_16x16x32_f16 v[88:91], v[22:25], v[56:59], v[88:91]
	s_waitcnt lgkmcnt(0)
	v_mfma_f32_16x16x32_f16 v[84:87], v[34:37], v[60:63], v[84:87]
	v_mfma_f32_16x16x32_f16 v[88:91], v[26:29], v[60:63], v[88:91]
	s_add_u32 s13, s12, 6
	s_min_u32 s13, s13, 450
	s_cmp_ge_u32 s14, s13
	s_cbranch_scc0 .Lca_slow_18
.Lca_ok_16:
	buffer_load_dwordx4 v[46:49], v117, s[4:7], 0 offen offset:3072 sc1
	ds_read_b128 v[50:53], v116 offset:1024
	s_setprio 0
	v_exp_f32_e32 v94, v86
	v_exp_f32_e32 v95, v90
	v_exp_f32_e32 v96, v84
	v_exp_f32_e32 v97, v88
	v_exp_f32_e32 v98, v85
	v_exp_f32_e32 v99, v89
	v_pk_add_f32 v[100:101], v[94:95], 1.0 op_sel_hi:[1,0]
	v_pk_fma_f32 v[102:103], v[94:95], s[8:9], v[92:93] op_sel_hi:[1,0,0]
	v_pk_fma_f32 v[100:101], v[96:97], v[100:101], v[100:101]
	v_pk_fma_f32 v[104:105], v[100:101], v[98:99], v[100:101]
	v_rcp_f32_e32 v104, v104
	v_rcp_f32_e32 v105, v105
	v_pk_fma_f32 v[102:103], v[102:103], v[98:99], v[102:103]
	v_pk_fma_f32 v[102:103], v[64:65], v[100:101], v[102:103]
	v_exp_f32_e32 v106, v87
	v_pk_mul_f32 v[64:65], v[102:103], v[104:105]
	v_exp_f32_e32 v108, v64
	v_exp_f32_e32 v109, v65
	v_exp_f32_e32 v107, v91
	v_pk_add_f32 v[110:111], v[108:109], 1.0 op_sel_hi:[1,0]
	v_pk_fma_f32 v[110:111], v[110:111], v[106:107], v[110:111]
	v_rcp_f32_e32 v110, v110
	v_rcp_f32_e32 v111, v111
	v_pk_add_f32 v[112:113], v[108:109], -1.0 op_sel_hi:[1,0]
	v_pk_mul_f32 v[112:113], v[112:113], v[110:111]
	v_cvt_pk_f16_f32 v114, v112, v113
	ds_write_b32 v81, v114 offset:2048
	s_waitcnt lgkmcnt(0)
	s_add_u32 s12, s12, 4
	v_add_u32_e32 v116, 0x400, v116
	v_add_u32_e32 v117, 0x1000, v117
	s_cmp_lt_u32 s12, 450
	s_cbranch_scc1 .Lca_loop
	s_barrier
	s_barrier
	s_barrier
	s_barrier
	s_endpgm
